# v037 + L3 rebalance: workgroups without a Fourier in-proj GEMM unit take four chunk-summary units each, the GEMM workgroups none
# speedup vs baseline: 1.0046x; 1.0046x over previous
; __global__ void __launch_bounds__(NTHR, 2) mk_fwd(Args args) {
;     ...
;             if (G == 256) {
;                 const int b_ = (int)blockIdx.x;
;                 for (int k = 0; k < ((b_ < 128) ? 3 : 1); ++k) { const int it = (b_ < 128) ? b_ + 128 + 128 * k : 384 + b_;
;                     m1_unit(lds, it - 128, (const bf16*)(ws + WS_Z), (const float*)(ws + WS_GATES), P.conv_w + (size_t)layer * 3 * 512, (float*)(ws + WS_CLOC), (float*)(ws + WS_SMALL), (float*)(ws + WS_SMALL) + 131072, 0); }
.LBB0_437:
	s_mov_b64 s[6:7], s[76:77]
	s_load_dwordx4 s[44:47], s[6:7], 0x40
	s_load_dwordx2 s[0:1], s[6:7], 0xd8
	v_readlane_b32 s4, v254, 15
	v_readlane_b32 s5, v254, 16
	s_andn2_b64 vcc, exec, s[4:5]
	s_mov_b64 s[8:9], -1
	s_cbranch_vccnz .LBB0_452
	s_waitcnt lgkmcnt(0)
	s_add_u32 s12, s0, 0x4e600000
	s_addc_u32 s13, s1, 0
	s_add_u32 s20, s0, 0x52600000
	s_mul_i32 s16, s86, 0x600
	s_addc_u32 s21, s1, 0
	s_lshl_b64 s[4:5], s[16:17], 2
	s_add_u32 s28, s46, s4
	s_addc_u32 s29, s47, s5
	s_add_u32 s30, s0, 0x55700000
	s_addc_u32 s31, s1, 0
	s_add_u32 s42, s0, 0x58700000
	s_addc_u32 s43, s1, 0
	s_add_u32 s48, s0, 0x58780000
	s_addc_u32 s49, s1, 0
	s_add_u32 s50, s28, 0x1000
	s_addc_u32 s51, s29, 0
	s_mov_b32 s5, 0
	v_readlane_b32 s4, v255, 5
	s_and_b64 vcc, exec, s[26:27]
	s_cbranch_vccz .LBB0_451
	s_branch .LBB0_440
.LBB0_439:
	s_or_b64 exec, exec, s[8:9]
	s_add_i32 s11, s5, 1
	s_cmp_lt_u32 s5, 3
	s_cselect_b64 s[8:9], -1, 0
	s_and_b64 s[8:9], s[26:27], s[8:9]
	s_addk_i32 s4, 0x80
	s_andn2_b64 vcc, exec, s[8:9]
	s_mov_b32 s5, s11
	s_barrier
	s_cbranch_vccnz .LBB0_451
